# union 3: final combine loop issues the second and third batch of expert-row loads right behind the first
# baseline (speedup 1.0000x reference)
.LBB0_1206:
	v_mov_b32_e32 v4, v127
	v_mov_b32_e32 v131, v126
	global_load_dwordx4 v[0:3], v5, s[14:15]
	global_load_dwordx4 v[6:9], v5, s[14:15] offset:16
	s_ashr_i32 s0, s42, 31
	s_lshr_b32 s0, s0, 20
	s_add_i32 s0, s42, s0
	s_lshr_b32 s0, s0, 12
	ds_read_b32 v10, v128
	s_mulk_i32 s0, 0x3000
	s_ashr_i32 s1, s0, 31
	s_lshl_b64 s[0:1], s[0:1], 2
	s_add_u32 s0, s2, s0
	s_addc_u32 s1, s3, s1
	s_waitcnt lgkmcnt(0)
	v_ashrrev_i32_e32 v11, 31, v10
	v_lshlrev_b64 v[10:11], 19, v[10:11]
	v_lshl_add_u64 v[10:11], s[10:11], 0, v[10:11]
	s_waitcnt vmcnt(0)
	v_readfirstlane_b32 s6, v0
	v_readfirstlane_b32 s7, v1
	v_readfirstlane_b32 s22, v2
	v_readfirstlane_b32 s26, v3
	v_readfirstlane_b32 s27, v6
	v_readfirstlane_b32 s29, v7
	v_readfirstlane_b32 s30, v8
	v_readfirstlane_b32 s31, v9
	s_bfe_u32 s33, s6, 0x100010
	s_lshl_b32 s6, s6, 11
	s_bfe_u32 s34, s7, 0x100010
	s_bfe_u32 s35, s22, 0x100010
	s_lshl_b32 s36, s22, 11
	s_bfe_u32 s37, s26, 0x100010
	s_bfe_u32 s38, s27, 0x100010
	s_bfe_u32 s39, s29, 0x100010
	s_bfe_u32 s40, s30, 0x100010
	s_bfe_u32 s41, s31, 0x100010
	s_lshl_b32 s33, s33, 2
	s_and_b32 s22, s6, 0x7fff800
	s_lshl_b32 s6, s34, 2
	s_lshl_b32 s34, s35, 2
	s_lshl_b32 s35, s37, 2
	s_lshl_b32 s37, s38, 2
	s_lshl_b32 s38, s39, 2
	s_lshl_b32 s39, s40, 2
	s_lshl_b32 s40, s41, 2
	s_add_i32 s33, s25, s33
	s_add_i32 s6, s25, s6
	s_add_i32 s34, s25, s34
	s_add_i32 s35, s25, s35
	s_add_i32 s37, s25, s37
	s_add_i32 s38, s25, s38
	s_add_i32 s39, s25, s39
	s_add_i32 s40, s25, s40
	v_mov_b32_e32 v0, s33
	v_mov_b32_e32 v1, s6
	v_readfirstlane_b32 s4, v10
	v_readfirstlane_b32 s5, v11
	v_mov_b32_e32 v3, s34
	v_mov_b32_e32 v7, s35
	v_mov_b32_e32 v9, s37
	v_mov_b32_e32 v11, s38
	v_mov_b32_e32 v13, s39
	v_mov_b32_e32 v15, s40
	ds_read_b32 v0, v0
	ds_read_b32 v2, v1
	ds_read_b32 v6, v3
	ds_read_b32 v8, v7
	ds_read_b32 v10, v9
	ds_read_b32 v12, v11
	ds_read_b32 v14, v13
	ds_read_b32 v18, v15
	s_waitcnt lgkmcnt(7)
	v_ashrrev_i32_e32 v1, 31, v0
	s_waitcnt lgkmcnt(6)
	v_ashrrev_i32_e32 v3, 31, v2
	v_lshlrev_b64 v[0:1], 19, v[0:1]
	s_lshl_b32 s7, s7, 11
	s_waitcnt lgkmcnt(5)
	v_ashrrev_i32_e32 v7, 31, v6
	v_lshlrev_b64 v[2:3], 19, v[2:3]
	v_lshl_add_u64 v[0:1], s[8:9], 0, v[0:1]
	s_waitcnt lgkmcnt(4)
	v_ashrrev_i32_e32 v9, 31, v8
	v_lshlrev_b64 v[6:7], 19, v[6:7]
	v_lshl_add_u64 v[2:3], s[8:9], 0, v[2:3]
	v_lshl_add_u64 v[136:137], v[0:1], 0, s[22:23]
	s_and_b32 s22, s7, 0x7fff800
	s_lshl_b32 s26, s26, 11
	s_waitcnt lgkmcnt(3)
	v_ashrrev_i32_e32 v11, 31, v10
	v_lshlrev_b64 v[8:9], 19, v[8:9]
	v_lshl_add_u64 v[6:7], s[8:9], 0, v[6:7]
	v_lshl_add_u64 v[140:141], v[2:3], 0, s[22:23]
	s_and_b32 s22, s36, 0x7fff800
	s_lshl_b32 s27, s27, 11
	s_waitcnt lgkmcnt(2)
	v_ashrrev_i32_e32 v13, 31, v12
	v_lshlrev_b64 v[10:11], 19, v[10:11]
	v_lshl_add_u64 v[8:9], s[8:9], 0, v[8:9]
	v_lshl_add_u64 v[148:149], v[6:7], 0, s[22:23]
	s_and_b32 s22, s26, 0x7fff800
	v_lshl_add_u64 v[10:11], s[8:9], 0, v[10:11]
	v_lshl_add_u64 v[64:65], v[8:9], 0, s[22:23]
	s_and_b32 s22, s27, 0x7fff800
	v_lshlrev_b64 v[6:7], 19, v[12:13]
	s_lshl_b32 s6, s29, 11
	v_lshl_add_u64 v[66:67], v[10:11], 0, s[22:23]
	s_and_b32 s22, s6, 0x7fff800
	v_lshl_add_u64 v[6:7], s[8:9], 0, v[6:7]
	s_waitcnt lgkmcnt(1)
	v_ashrrev_i32_e32 v15, 31, v14
	global_load_dwordx4 v[0:3], v131, s[4:5]
	v_lshl_add_u64 v[78:79], v[6:7], 0, s[22:23]
	v_lshlrev_b64 v[6:7], 19, v[14:15]
	global_load_dwordx4 v[14:17], v131, s[4:5] offset:1024
	s_lshl_b32 s4, s30, 11
	s_and_b32 s22, s4, 0x7fff800
	v_lshl_add_u64 v[6:7], s[8:9], 0, v[6:7]
	v_lshl_add_u64 v[6:7], v[6:7], 0, s[22:23]
	s_waitcnt lgkmcnt(0)
	v_ashrrev_i32_e32 v19, 31, v18
	v_readfirstlane_b32 s4, v6
	v_readfirstlane_b32 s5, v7
	v_lshlrev_b64 v[6:7], 19, v[18:19]
	v_lshl_add_u64 v[6:7], s[8:9], 0, v[6:7]
	s_waitcnt vmcnt(1)
	v_cvt_pk_f32_fp8_e32 v[110:111], v0
	s_nop 0
	global_load_dwordx4 v[10:13], v131, s[4:5]
	global_load_dwordx4 v[24:27], v131, s[4:5] offset:1024
	s_lshl_b32 s4, s31, 11
	s_and_b32 s22, s4, 0x7fff800
	v_lshl_add_u64 v[6:7], v[6:7], 0, s[22:23]
	s_add_u32 s0, s0, 0x10a000
	v_readfirstlane_b32 s4, v6
	v_readfirstlane_b32 s5, v7
	s_nop 4
	global_load_dwordx4 v[38:41], v131, s[4:5]
	global_load_dwordx4 v[50:53], v131, s[4:5] offset:1024
	v_readfirstlane_b32 s26, v64
	v_readfirstlane_b32 s27, v65
	s_nop 4
	global_load_dwordx4 v[244:247], v131, s[26:27]
	global_load_dwordx4 v[70:73], v131, s[26:27] offset:1024
	v_readfirstlane_b32 s26, v66
	v_readfirstlane_b32 s27, v67
	s_nop 4
	global_load_dwordx4 v[82:85], v131, s[26:27]
	global_load_dwordx4 v[86:89], v131, s[26:27] offset:1024
	v_readfirstlane_b32 s26, v78
	v_readfirstlane_b32 s27, v79
	s_nop 4
	global_load_dwordx4 v[102:105], v131, s[26:27]
	global_load_dwordx4 v[132:135], v131, s[26:27] offset:1024
	v_readfirstlane_b32 s26, v136
	v_readfirstlane_b32 s27, v137
	s_nop 4
	global_load_dwordx4 v[248:251], v131, s[26:27]
	global_load_dwordx4 v[136:139], v131, s[26:27] offset:1024
	v_readfirstlane_b32 s26, v140
	v_readfirstlane_b32 s27, v141
	s_nop 4
	global_load_dwordx4 v[140:143], v131, s[26:27]
	global_load_dwordx4 v[144:147], v131, s[26:27] offset:1024
	v_readfirstlane_b32 s26, v148
	v_readfirstlane_b32 s27, v149
	s_nop 4
	global_load_dwordx4 v[148:151], v131, s[26:27]
	global_load_dwordx4 v[252:255], v131, s[26:27] offset:1024
	s_load_dwordx4 s[4:7], s[96:97], 0xa8
	v_cvt_pk_f32_fp8_sdwa v[116:117], v0 src0_sel:WORD_1
	v_cvt_pk_f32_fp8_e32 v[112:113], v1
	v_cvt_pk_f32_fp8_sdwa v[118:119], v1 src0_sel:WORD_1
	v_cvt_pk_f32_fp8_e32 v[54:55], v2
	v_cvt_pk_f32_fp8_sdwa v[60:61], v2 src0_sel:WORD_1
	v_cvt_pk_f32_fp8_e32 v[42:43], v3
	v_cvt_pk_f32_fp8_sdwa v[44:45], v3 src0_sel:WORD_1
	s_waitcnt vmcnt(16)
	v_cvt_pk_f32_fp8_e32 v[30:31], v14
	v_cvt_pk_f32_fp8_sdwa v[32:33], v14 src0_sel:WORD_1
	v_cvt_pk_f32_fp8_e32 v[18:19], v15
	v_cvt_pk_f32_fp8_sdwa v[22:23], v15 src0_sel:WORD_1
	v_cvt_pk_f32_fp8_e32 v[2:3], v16
	v_cvt_pk_f32_fp8_sdwa v[8:9], v16 src0_sel:WORD_1
	v_cvt_pk_f32_fp8_e32 v[0:1], v17
	v_cvt_pk_f32_fp8_sdwa v[16:17], v17 src0_sel:WORD_1
	s_addc_u32 s1, s1, 0
	s_waitcnt vmcnt(15)
	v_cvt_pk_f32_fp8_e32 v[152:153], v10
	v_cvt_pk_f32_fp8_sdwa v[154:155], v10 src0_sel:WORD_1
	v_cvt_pk_f32_fp8_e32 v[156:157], v11
	v_cvt_pk_f32_fp8_sdwa v[158:159], v11 src0_sel:WORD_1
	v_cvt_pk_f32_fp8_e32 v[160:161], v12
	v_cvt_pk_f32_fp8_sdwa v[162:163], v12 src0_sel:WORD_1
	v_cvt_pk_f32_fp8_e32 v[62:63], v13
	v_cvt_pk_f32_fp8_sdwa v[68:69], v13 src0_sel:WORD_1
	s_waitcnt vmcnt(14)
	v_cvt_pk_f32_fp8_e32 v[46:47], v24
	v_cvt_pk_f32_fp8_sdwa v[48:49], v24 src0_sel:WORD_1
	v_cvt_pk_f32_fp8_e32 v[34:35], v25
	v_cvt_pk_f32_fp8_sdwa v[36:37], v25 src0_sel:WORD_1
	v_cvt_pk_f32_fp8_e32 v[20:21], v26
	v_cvt_pk_f32_fp8_sdwa v[24:25], v26 src0_sel:WORD_1
	v_cvt_pk_f32_fp8_e32 v[6:7], v27
	v_cvt_pk_f32_fp8_sdwa v[10:11], v27 src0_sel:WORD_1
	s_waitcnt vmcnt(13)
	v_cvt_pk_f32_fp8_e32 v[164:165], v38
	v_cvt_pk_f32_fp8_sdwa v[166:167], v38 src0_sel:WORD_1
	v_cvt_pk_f32_fp8_e32 v[168:169], v39
	v_cvt_pk_f32_fp8_sdwa v[170:171], v39 src0_sel:WORD_1
	v_cvt_pk_f32_fp8_e32 v[90:91], v40
	v_cvt_pk_f32_fp8_sdwa v[92:93], v40 src0_sel:WORD_1
	v_cvt_pk_f32_fp8_e32 v[74:75], v41
	v_cvt_pk_f32_fp8_sdwa v[76:77], v41 src0_sel:WORD_1
	s_waitcnt vmcnt(12)
	v_cvt_pk_f32_fp8_e32 v[56:57], v50
	v_cvt_pk_f32_fp8_sdwa v[58:59], v50 src0_sel:WORD_1
	v_cvt_pk_f32_fp8_e32 v[38:39], v51
	v_cvt_pk_f32_fp8_sdwa v[40:41], v51 src0_sel:WORD_1
	v_cvt_pk_f32_fp8_e32 v[26:27], v52
	v_cvt_pk_f32_fp8_sdwa v[28:29], v52 src0_sel:WORD_1
	v_cvt_pk_f32_fp8_e32 v[12:13], v53
	v_cvt_pk_f32_fp8_sdwa v[14:15], v53 src0_sel:WORD_1
	s_waitcnt vmcnt(11)
	v_cvt_pk_f32_fp8_e32 v[172:173], v244
	v_cvt_pk_f32_fp8_sdwa v[174:175], v244 src0_sel:WORD_1
	v_cvt_pk_f32_fp8_e32 v[176:177], v245
	v_cvt_pk_f32_fp8_sdwa v[178:179], v245 src0_sel:WORD_1
	v_cvt_pk_f32_fp8_e32 v[180:181], v246
	v_cvt_pk_f32_fp8_sdwa v[182:183], v246 src0_sel:WORD_1
	v_cvt_pk_f32_fp8_e32 v[106:107], v247
	v_cvt_pk_f32_fp8_sdwa v[108:109], v247 src0_sel:WORD_1
	s_waitcnt vmcnt(10)
	v_cvt_pk_f32_fp8_e32 v[94:95], v70
	v_cvt_pk_f32_fp8_sdwa v[96:97], v70 src0_sel:WORD_1
	v_cvt_pk_f32_fp8_e32 v[78:79], v71
	v_cvt_pk_f32_fp8_sdwa v[80:81], v71 src0_sel:WORD_1
	v_cvt_pk_f32_fp8_e32 v[64:65], v72
	v_cvt_pk_f32_fp8_sdwa v[66:67], v72 src0_sel:WORD_1
	v_cvt_pk_f32_fp8_e32 v[50:51], v73
	v_cvt_pk_f32_fp8_sdwa v[52:53], v73 src0_sel:WORD_1
	s_waitcnt vmcnt(9)
	v_cvt_pk_f32_fp8_e32 v[184:185], v82
	v_cvt_pk_f32_fp8_sdwa v[186:187], v82 src0_sel:WORD_1
	v_cvt_pk_f32_fp8_e32 v[188:189], v83
	v_cvt_pk_f32_fp8_sdwa v[190:191], v83 src0_sel:WORD_1
	v_cvt_pk_f32_fp8_e32 v[192:193], v84
	v_cvt_pk_f32_fp8_sdwa v[194:195], v84 src0_sel:WORD_1
	v_cvt_pk_f32_fp8_e32 v[196:197], v85
	v_cvt_pk_f32_fp8_sdwa v[198:199], v85 src0_sel:WORD_1
	s_waitcnt vmcnt(8)
	v_cvt_pk_f32_fp8_e32 v[114:115], v86
	v_cvt_pk_f32_fp8_sdwa v[120:121], v86 src0_sel:WORD_1
	v_cvt_pk_f32_fp8_e32 v[98:99], v87
	v_cvt_pk_f32_fp8_sdwa v[100:101], v87 src0_sel:WORD_1
	v_cvt_pk_f32_fp8_e32 v[82:83], v88
	v_cvt_pk_f32_fp8_sdwa v[84:85], v88 src0_sel:WORD_1
	v_cvt_pk_f32_fp8_e32 v[70:71], v89
	v_cvt_pk_f32_fp8_sdwa v[72:73], v89 src0_sel:WORD_1
	s_waitcnt vmcnt(7)
	v_cvt_pk_f32_fp8_e32 v[200:201], v102
	v_cvt_pk_f32_fp8_sdwa v[202:203], v102 src0_sel:WORD_1
	v_cvt_pk_f32_fp8_e32 v[204:205], v103
	v_cvt_pk_f32_fp8_sdwa v[206:207], v103 src0_sel:WORD_1
	v_cvt_pk_f32_fp8_e32 v[208:209], v104
	v_cvt_pk_f32_fp8_sdwa v[210:211], v104 src0_sel:WORD_1
	v_cvt_pk_f32_fp8_e32 v[212:213], v105
	v_cvt_pk_f32_fp8_sdwa v[214:215], v105 src0_sel:WORD_1
	s_waitcnt vmcnt(6)
	v_cvt_pk_f32_fp8_e32 v[216:217], v132
	v_cvt_pk_f32_fp8_sdwa v[218:219], v132 src0_sel:WORD_1
	v_cvt_pk_f32_fp8_e32 v[122:123], v133
	v_cvt_pk_f32_fp8_sdwa v[124:125], v133 src0_sel:WORD_1
	v_cvt_pk_f32_fp8_e32 v[102:103], v134
	v_cvt_pk_f32_fp8_sdwa v[104:105], v134 src0_sel:WORD_1
	v_cvt_pk_f32_fp8_e32 v[86:87], v135
	v_cvt_pk_f32_fp8_sdwa v[88:89], v135 src0_sel:WORD_1
	v_pk_add_f32 v[220:221], v[154:155], 0 op_sel_hi:[1,0]
	v_pk_add_f32 v[222:223], v[152:153], 0 op_sel_hi:[1,0]
	v_pk_add_f32 v[158:159], v[158:159], 0 op_sel_hi:[1,0]
	v_pk_add_f32 v[164:165], v[164:165], v[222:223]
	v_pk_add_f32 v[158:159], v[170:171], v[158:159]
	v_pk_add_f32 v[110:111], v[110:111], v[164:165]
	v_pk_add_f32 v[24:25], v[24:25], 0 op_sel_hi:[1,0]
	v_pk_add_f32 v[20:21], v[20:21], 0 op_sel_hi:[1,0]
	v_pk_add_f32 v[118:119], v[118:119], v[158:159]
	v_pk_add_f32 v[110:111], v[172:173], v[110:111]
	v_pk_add_f32 v[20:21], v[26:27], v[20:21]
	v_pk_add_f32 v[24:25], v[28:29], v[24:25]
	v_pk_add_f32 v[156:157], v[156:157], 0 op_sel_hi:[1,0]
	v_pk_add_f32 v[118:119], v[178:179], v[118:119]
	v_pk_add_f32 v[110:111], v[184:185], v[110:111]
	v_pk_add_f32 v[36:37], v[36:37], 0 op_sel_hi:[1,0]
	v_pk_add_f32 v[34:35], v[34:35], 0 op_sel_hi:[1,0]
	v_pk_add_f32 v[8:9], v[8:9], v[24:25]
	v_pk_add_f32 v[2:3], v[2:3], v[20:21]
	v_pk_add_f32 v[166:167], v[166:167], v[220:221]
	v_pk_add_f32 v[156:157], v[168:169], v[156:157]
	v_pk_add_f32 v[34:35], v[38:39], v[34:35]
	v_pk_add_f32 v[36:37], v[40:41], v[36:37]
	v_pk_add_f32 v[2:3], v[64:65], v[2:3]
	v_pk_add_f32 v[8:9], v[66:67], v[8:9]
	v_pk_add_f32 v[162:163], v[162:163], 0 op_sel_hi:[1,0]
	v_pk_add_f32 v[160:161], v[160:161], 0 op_sel_hi:[1,0]
	v_pk_add_f32 v[116:117], v[116:117], v[166:167]
	v_pk_add_f32 v[112:113], v[112:113], v[156:157]
	v_pk_add_f32 v[68:69], v[68:69], 0 op_sel_hi:[1,0]
	v_pk_add_f32 v[62:63], v[62:63], 0 op_sel_hi:[1,0]
	v_pk_add_f32 v[48:49], v[48:49], 0 op_sel_hi:[1,0]
	v_pk_add_f32 v[46:47], v[46:47], 0 op_sel_hi:[1,0]
	v_pk_add_f32 v[22:23], v[22:23], v[36:37]
	v_pk_add_f32 v[18:19], v[18:19], v[34:35]
	v_pk_add_f32 v[8:9], v[84:85], v[8:9]
	v_pk_add_f32 v[2:3], v[82:83], v[2:3]
	v_pk_add_f32 v[10:11], v[10:11], 0 op_sel_hi:[1,0]
	v_pk_add_f32 v[6:7], v[6:7], 0 op_sel_hi:[1,0]
	v_pk_add_f32 v[116:117], v[174:175], v[116:117]
	v_pk_add_f32 v[112:113], v[176:177], v[112:113]
	v_pk_add_f32 v[90:91], v[90:91], v[160:161]
	v_pk_add_f32 v[92:93], v[92:93], v[162:163]
	v_pk_add_f32 v[62:63], v[74:75], v[62:63]
	v_pk_add_f32 v[68:69], v[76:77], v[68:69]
	v_pk_add_f32 v[46:47], v[56:57], v[46:47]
	v_pk_add_f32 v[48:49], v[58:59], v[48:49]
	v_pk_add_f32 v[2:3], v[102:103], v[2:3]
	v_pk_add_f32 v[8:9], v[104:105], v[8:9]
	v_pk_add_f32 v[6:7], v[12:13], v[6:7]
	v_pk_add_f32 v[10:11], v[14:15], v[10:11]
	v_pk_add_f32 v[116:117], v[186:187], v[116:117]
	v_pk_add_f32 v[118:119], v[190:191], v[118:119]
	v_pk_add_f32 v[112:113], v[188:189], v[112:113]
	v_pk_add_f32 v[60:61], v[60:61], v[92:93]
	v_pk_add_f32 v[54:55], v[54:55], v[90:91]
	v_pk_add_f32 v[44:45], v[44:45], v[68:69]
	v_pk_add_f32 v[42:43], v[42:43], v[62:63]
	v_pk_add_f32 v[32:33], v[32:33], v[48:49]
	v_pk_add_f32 v[30:31], v[30:31], v[46:47]
	v_pk_add_f32 v[10:11], v[16:17], v[10:11]
	v_pk_add_f32 v[0:1], v[0:1], v[6:7]
	v_pk_add_f32 v[110:111], v[200:201], v[110:111]
	v_pk_add_f32 v[116:117], v[202:203], v[116:117]
	v_pk_add_f32 v[112:113], v[204:205], v[112:113]
	v_pk_add_f32 v[118:119], v[206:207], v[118:119]
	v_pk_add_f32 v[54:55], v[180:181], v[54:55]
	v_pk_add_f32 v[60:61], v[182:183], v[60:61]
	v_pk_add_f32 v[42:43], v[106:107], v[42:43]
	v_pk_add_f32 v[44:45], v[108:109], v[44:45]
	v_pk_add_f32 v[30:31], v[94:95], v[30:31]
	s_waitcnt vmcnt(5)
	v_cvt_pk_f32_fp8_e32 v[156:157], v248
	s_waitcnt vmcnt(4)
	v_cvt_pk_f32_fp8_e32 v[178:179], v138
	v_cvt_pk_f32_fp8_sdwa v[184:185], v138 src0_sel:WORD_1
	v_cvt_pk_f32_fp8_sdwa v[158:159], v248 src0_sel:WORD_1
	s_waitcnt vmcnt(2)
	v_cvt_pk_f32_fp8_e32 v[226:227], v146
	v_cvt_pk_f32_fp8_sdwa v[228:229], v146 src0_sel:WORD_1
	v_cvt_pk_f32_fp8_e32 v[164:165], v249
	v_cvt_pk_f32_fp8_sdwa v[132:133], v249 src0_sel:WORD_1
	v_cvt_pk_f32_fp8_e32 v[166:167], v250
	v_cvt_pk_f32_fp8_sdwa v[168:169], v250 src0_sel:WORD_1
	v_cvt_pk_f32_fp8_e32 v[170:171], v251
	v_cvt_pk_f32_fp8_sdwa v[134:135], v251 src0_sel:WORD_1
	v_cvt_pk_f32_fp8_e32 v[172:173], v136
	s_waitcnt vmcnt(0)
	v_cvt_pk_f32_fp8_e32 v[34:35], v254
	v_cvt_pk_f32_fp8_sdwa v[36:37], v254 src0_sel:WORD_1
	v_cvt_pk_f32_fp8_sdwa v[174:175], v136 src0_sel:WORD_1
	v_cvt_pk_f32_fp8_e32 v[176:177], v137
	v_cvt_pk_f32_fp8_sdwa v[136:137], v137 src0_sel:WORD_1
	v_cvt_pk_f32_fp8_e32 v[186:187], v139
	v_cvt_pk_f32_fp8_sdwa v[138:139], v139 src0_sel:WORD_1
	v_pk_add_f32 v[8:9], v[184:185], v[8:9]
	v_pk_add_f32 v[2:3], v[178:179], v[2:3]
	v_cvt_pk_f32_fp8_e32 v[188:189], v140
	v_cvt_pk_f32_fp8_sdwa v[190:191], v140 src0_sel:WORD_1
	v_cvt_pk_f32_fp8_e32 v[200:201], v141
	v_cvt_pk_f32_fp8_sdwa v[140:141], v141 src0_sel:WORD_1
	v_cvt_pk_f32_fp8_e32 v[202:203], v142
	v_cvt_pk_f32_fp8_sdwa v[204:205], v142 src0_sel:WORD_1
	v_cvt_pk_f32_fp8_e32 v[206:207], v143
	v_cvt_pk_f32_fp8_sdwa v[142:143], v143 src0_sel:WORD_1
	v_cvt_pk_f32_fp8_e32 v[220:221], v144
	v_cvt_pk_f32_fp8_sdwa v[222:223], v144 src0_sel:WORD_1
	v_cvt_pk_f32_fp8_e32 v[224:225], v145
	v_cvt_pk_f32_fp8_sdwa v[144:145], v145 src0_sel:WORD_1
	v_cvt_pk_f32_fp8_e32 v[230:231], v147
	v_cvt_pk_f32_fp8_sdwa v[146:147], v147 src0_sel:WORD_1
	v_pk_add_f32 v[32:33], v[96:97], v[32:33]
	v_pk_add_f32 v[18:19], v[78:79], v[18:19]
	v_pk_add_f32 v[22:23], v[80:81], v[22:23]
	v_pk_add_f32 v[2:3], v[226:227], v[2:3]
	v_pk_add_f32 v[8:9], v[228:229], v[8:9]
	v_pk_add_f32 v[0:1], v[50:51], v[0:1]
	v_pk_add_f32 v[6:7], v[52:53], v[10:11]
	v_cvt_pk_f32_fp8_e32 v[232:233], v148
	v_cvt_pk_f32_fp8_sdwa v[234:235], v148 src0_sel:WORD_1
	v_cvt_pk_f32_fp8_e32 v[236:237], v149
	v_cvt_pk_f32_fp8_sdwa v[148:149], v149 src0_sel:WORD_1
	v_cvt_pk_f32_fp8_e32 v[238:239], v150
	v_cvt_pk_f32_fp8_sdwa v[240:241], v150 src0_sel:WORD_1
	v_pk_add_f32 v[60:61], v[194:195], v[60:61]
	v_pk_add_f32 v[54:55], v[192:193], v[54:55]
	v_cvt_pk_f32_fp8_e32 v[90:91], v151
	v_cvt_pk_f32_fp8_sdwa v[92:93], v151 src0_sel:WORD_1
	v_pk_add_f32 v[44:45], v[198:199], v[44:45]
	v_pk_add_f32 v[42:43], v[196:197], v[42:43]
	v_cvt_pk_f32_fp8_e32 v[62:63], v252
	v_cvt_pk_f32_fp8_sdwa v[68:69], v252 src0_sel:WORD_1
	v_pk_add_f32 v[32:33], v[120:121], v[32:33]
	v_pk_add_f32 v[30:31], v[114:115], v[30:31]
	v_cvt_pk_f32_fp8_e32 v[46:47], v253
	v_cvt_pk_f32_fp8_sdwa v[48:49], v253 src0_sel:WORD_1
	v_pk_add_f32 v[22:23], v[100:101], v[22:23]
	v_pk_add_f32 v[18:19], v[98:99], v[18:19]
	v_pk_add_f32 v[20:21], v[36:37], v[8:9]
	v_pk_add_f32 v[24:25], v[34:35], v[2:3]
	v_cvt_pk_f32_fp8_e32 v[2:3], v255
	v_cvt_pk_f32_fp8_sdwa v[8:9], v255 src0_sel:WORD_1
	v_pk_add_f32 v[6:7], v[72:73], v[6:7]
	v_pk_add_f32 v[0:1], v[70:71], v[0:1]
	v_pk_add_f32 v[54:55], v[208:209], v[54:55]
	v_pk_add_f32 v[60:61], v[210:211], v[60:61]
	v_pk_add_f32 v[42:43], v[212:213], v[42:43]
	v_pk_add_f32 v[44:45], v[214:215], v[44:45]
	v_pk_add_f32 v[30:31], v[216:217], v[30:31]
	v_pk_add_f32 v[32:33], v[218:219], v[32:33]
	v_pk_add_f32 v[18:19], v[122:123], v[18:19]
	v_pk_add_f32 v[22:23], v[124:125], v[22:23]
	v_pk_add_f32 v[0:1], v[86:87], v[0:1]
	v_pk_add_f32 v[6:7], v[88:89], v[6:7]
	v_pk_add_f32 v[116:117], v[158:159], v[116:117]
	v_pk_add_f32 v[110:111], v[156:157], v[110:111]
	v_pk_add_f32 v[118:119], v[132:133], v[118:119]
	v_pk_add_f32 v[112:113], v[164:165], v[112:113]
	v_pk_add_f32 v[60:61], v[168:169], v[60:61]
	v_pk_add_f32 v[54:55], v[166:167], v[54:55]
	v_pk_add_f32 v[44:45], v[134:135], v[44:45]
	v_pk_add_f32 v[42:43], v[170:171], v[42:43]
	v_pk_add_f32 v[32:33], v[174:175], v[32:33]
	v_pk_add_f32 v[30:31], v[172:173], v[30:31]
	v_pk_add_f32 v[22:23], v[136:137], v[22:23]
	v_pk_add_f32 v[18:19], v[176:177], v[18:19]
	v_pk_add_f32 v[6:7], v[138:139], v[6:7]
	v_pk_add_f32 v[0:1], v[186:187], v[0:1]
	v_pk_add_f32 v[110:111], v[188:189], v[110:111]
	v_pk_add_f32 v[116:117], v[190:191], v[116:117]
	v_pk_add_f32 v[112:113], v[200:201], v[112:113]
	v_pk_add_f32 v[118:119], v[140:141], v[118:119]
	v_pk_add_f32 v[54:55], v[202:203], v[54:55]
	v_pk_add_f32 v[60:61], v[204:205], v[60:61]
	v_pk_add_f32 v[42:43], v[206:207], v[42:43]
	v_pk_add_f32 v[44:45], v[142:143], v[44:45]
	v_pk_add_f32 v[30:31], v[220:221], v[30:31]
	v_pk_add_f32 v[32:33], v[222:223], v[32:33]
	v_pk_add_f32 v[18:19], v[224:225], v[18:19]
	v_pk_add_f32 v[22:23], v[144:145], v[22:23]
	v_pk_add_f32 v[0:1], v[230:231], v[0:1]
	v_pk_add_f32 v[6:7], v[146:147], v[6:7]
	v_pk_add_f32 v[116:117], v[234:235], v[116:117]
	v_pk_add_f32 v[110:111], v[232:233], v[110:111]
	v_pk_add_f32 v[118:119], v[148:149], v[118:119]
	v_pk_add_f32 v[112:113], v[236:237], v[112:113]
	v_pk_add_f32 v[60:61], v[240:241], v[60:61]
	v_pk_add_f32 v[54:55], v[238:239], v[54:55]
	v_pk_add_f32 v[44:45], v[92:93], v[44:45]
	v_pk_add_f32 v[42:43], v[90:91], v[42:43]
	v_pk_add_f32 v[32:33], v[68:69], v[32:33]
	v_pk_add_f32 v[30:31], v[62:63], v[30:31]
	v_pk_add_f32 v[22:23], v[48:49], v[22:23]
	v_pk_add_f32 v[18:19], v[46:47], v[18:19]
	v_pk_add_f32 v[34:35], v[8:9], v[6:7]
	v_pk_add_f32 v[36:37], v[2:3], v[0:1]
	s_waitcnt lgkmcnt(0)
	v_lshl_add_u64 v[38:39], s[6:7], 0, v[4:5]
	v_add_u32_e32 v6, 16, v4
	v_add_u32_e32 v8, 32, v4
	v_add_u32_e32 v12, 0x1000, v4
	v_add_u32_e32 v16, 0x1020, v4
	v_lshl_add_u64 v[122:123], v[38:39], 0, s[18:19]
	global_load_dwordx4 v[0:3], v4, s[0:1]
	v_pk_mul_f32 v[26:27], v[110:111], s[24:25] op_sel_hi:[1,0]
	v_pk_mul_f32 v[96:97], v[118:119], s[24:25] op_sel_hi:[1,0]
	v_pk_mul_f32 v[98:99], v[54:55], s[24:25] op_sel_hi:[1,0]
	v_pk_mul_f32 v[100:101], v[60:61], s[24:25] op_sel_hi:[1,0]
	v_add_u32_e32 v10, 48, v4
	v_pk_mul_f32 v[102:103], v[42:43], s[24:25] op_sel_hi:[1,0]
	v_pk_mul_f32 v[104:105], v[44:45], s[24:25] op_sel_hi:[1,0]
	v_pk_mul_f32 v[106:107], v[30:31], s[24:25] op_sel_hi:[1,0]
	v_pk_mul_f32 v[108:109], v[32:33], s[24:25] op_sel_hi:[1,0]
	v_add_u32_e32 v14, 0x1010, v4
	v_pk_mul_f32 v[110:111], v[18:19], s[24:25] op_sel_hi:[1,0]
	v_add_u32_e32 v18, 0x1030, v4
	v_pk_mul_f32 v[118:119], v[36:37], s[24:25] op_sel_hi:[1,0]
	v_pk_mul_f32 v[120:121], v[34:35], s[24:25] op_sel_hi:[1,0]
	global_load_dwordx4 v[30:33], v6, s[0:1]
	global_load_dwordx4 v[34:37], v8, s[0:1]
	global_load_dwordx4 v[38:41], v10, s[0:1]
	global_load_dwordx4 v[42:45], v12, s[0:1]
	global_load_dwordx4 v[46:49], v14, s[0:1]
	global_load_dwordx4 v[50:53], v16, s[0:1]
	global_load_dwordx4 v[54:57], v18, s[0:1]
	global_load_dwordx4 v[58:61], v[122:123], off
	v_mov_b32_e32 v7, v5
	v_pk_mul_f32 v[28:29], v[116:117], s[24:25] op_sel_hi:[1,0]
	v_mov_b32_e32 v9, v5
	v_mov_b32_e32 v11, v5
	v_mov_b32_e32 v13, v5
	v_mov_b32_e32 v15, v5
	v_mov_b32_e32 v17, v5
	v_pk_mul_f32 v[116:117], v[20:21], s[24:25] op_sel_hi:[1,0]
	v_mov_b32_e32 v19, v5
	v_lshl_add_u64 v[20:21], s[6:7], 0, v[6:7]
	v_pk_mul_f32 v[94:95], v[112:113], s[24:25] op_sel_hi:[1,0]
	v_pk_mul_f32 v[112:113], v[22:23], s[24:25] op_sel_hi:[1,0]
	v_pk_mul_f32 v[114:115], v[24:25], s[24:25] op_sel_hi:[1,0]
	v_lshl_add_u64 v[22:23], s[6:7], 0, v[8:9]
	v_lshl_add_u64 v[24:25], s[6:7], 0, v[10:11]
	v_lshl_add_u64 v[62:63], s[6:7], 0, v[12:13]
	v_lshl_add_u64 v[64:65], s[6:7], 0, v[14:15]
	v_lshl_add_u64 v[66:67], s[6:7], 0, v[16:17]
	v_lshl_add_u64 v[68:69], s[6:7], 0, v[18:19]
	v_lshl_add_u64 v[124:125], v[20:21], 0, s[18:19]
	v_lshl_add_u64 v[132:133], v[22:23], 0, s[18:19]
	v_lshl_add_u64 v[134:135], v[24:25], 0, s[18:19]
	v_lshl_add_u64 v[136:137], v[62:63], 0, s[18:19]
	v_lshl_add_u64 v[24:25], v[64:65], 0, s[18:19]
	v_lshl_add_u64 v[22:23], v[66:67], 0, s[18:19]
	v_lshl_add_u64 v[20:21], v[68:69], 0, s[18:19]
	global_load_dwordx4 v[62:65], v[124:125], off
	global_load_dwordx4 v[66:69], v[132:133], off
	global_load_dwordx4 v[70:73], v[134:135], off
	global_load_dwordx4 v[74:77], v[136:137], off
	global_load_dwordx4 v[78:81], v[24:25], off
	global_load_dwordx4 v[82:85], v[22:23], off
	global_load_dwordx4 v[86:89], v[20:21], off
	global_load_dwordx4 v[90:93], v4, s[4:5]
	s_add_i32 s42, s42, s56
	s_add_u32 s10, s10, s12
	s_addc_u32 s11, s11, s13
	s_add_u32 s14, s14, s16
	s_addc_u32 s15, s15, s17
	s_add_u32 s18, s18, s20
	s_addc_u32 s19, s19, s21
	s_cmpk_lt_i32 s42, 0x2000
	s_waitcnt vmcnt(8)
	v_pk_fma_f32 v[2:3], v[2:3], v[28:29], v[60:61]
	v_pk_fma_f32 v[0:1], v[0:1], v[26:27], v[58:59]
	v_mul_f32_e32 v7, v3, v3
	v_mul_f32_e32 v4, v1, v1
	v_fmac_f32_e32 v4, v0, v0
	v_fmac_f32_e32 v7, v2, v2
	v_add_f32_e32 v4, v4, v7
	s_waitcnt vmcnt(7)
	v_pk_fma_f32 v[26:27], v[32:33], v[96:97], v[64:65]
	v_pk_fma_f32 v[28:29], v[30:31], v[94:95], v[62:63]
	s_waitcnt vmcnt(6)
	v_pk_fma_f32 v[30:31], v[36:37], v[100:101], v[68:69]
	v_pk_fma_f32 v[32:33], v[34:35], v[98:99], v[66:67]
	v_mul_f32_e32 v9, v29, v29
	v_mul_f32_e32 v11, v27, v27
	s_waitcnt vmcnt(5)
	v_pk_fma_f32 v[34:35], v[40:41], v[104:105], v[72:73]
	v_pk_fma_f32 v[36:37], v[38:39], v[102:103], v[70:71]
	v_mul_f32_e32 v13, v33, v33
	v_mul_f32_e32 v15, v31, v31
	v_fmac_f32_e32 v9, v28, v28
	v_fmac_f32_e32 v11, v26, v26
	s_waitcnt vmcnt(4)
	v_pk_fma_f32 v[38:39], v[44:45], v[108:109], v[76:77]
	v_pk_fma_f32 v[40:41], v[42:43], v[106:107], v[74:75]
	v_mul_f32_e32 v17, v37, v37
	v_mul_f32_e32 v19, v35, v35
	v_fmac_f32_e32 v13, v32, v32
	v_fmac_f32_e32 v15, v30, v30
	v_add_f32_e32 v7, v9, v11
	s_waitcnt vmcnt(3)
	v_pk_fma_f32 v[42:43], v[48:49], v[112:113], v[80:81]
	v_pk_fma_f32 v[44:45], v[46:47], v[110:111], v[78:79]
	s_waitcnt vmcnt(2)
	v_pk_fma_f32 v[46:47], v[52:53], v[116:117], v[84:85]
	s_waitcnt vmcnt(1)
	v_pk_fma_f32 v[52:53], v[54:55], v[118:119], v[86:87]
	v_mul_f32_e32 v54, v41, v41
	v_mul_f32_e32 v55, v39, v39
	v_fmac_f32_e32 v17, v36, v36
	v_fmac_f32_e32 v19, v34, v34
	v_add_f32_e32 v9, v13, v15
	v_add_f32_e32 v4, v4, v7
	v_pk_fma_f32 v[48:49], v[50:51], v[114:115], v[82:83]
	v_pk_fma_f32 v[50:51], v[56:57], v[120:121], v[88:89]
	v_mul_f32_e32 v56, v45, v45
	v_mul_f32_e32 v57, v43, v43
	v_fmac_f32_e32 v54, v40, v40
	v_fmac_f32_e32 v55, v38, v38
	v_add_f32_e32 v11, v17, v19
	v_add_f32_e32 v4, v4, v9
	v_mul_f32_e32 v58, v49, v49
	v_mul_f32_e32 v59, v47, v47
	v_fmac_f32_e32 v56, v44, v44
	v_fmac_f32_e32 v57, v42, v42
	v_add_f32_e32 v13, v54, v55
	v_add_f32_e32 v4, v4, v11
	v_mul_f32_e32 v60, v53, v53
	v_mul_f32_e32 v61, v51, v51
	v_fmac_f32_e32 v58, v48, v48
	v_fmac_f32_e32 v59, v46, v46
	v_add_f32_e32 v15, v56, v57
	v_add_f32_e32 v4, v4, v13
	v_fmac_f32_e32 v60, v52, v52
	v_fmac_f32_e32 v61, v50, v50
	v_add_f32_e32 v17, v58, v59
	v_add_f32_e32 v4, v4, v15
	v_add_f32_e32 v19, v60, v61
	v_add_f32_e32 v4, v4, v17
	v_add_f32_e32 v4, v4, v19
	ds_swizzle_b32 v7, v4 offset:swizzle(SWAP,1)
	s_waitcnt lgkmcnt(0)
	v_add_f32_e32 v4, v4, v7
	ds_swizzle_b32 v7, v4 offset:swizzle(SWAP,2)
	s_waitcnt lgkmcnt(0)
	v_add_f32_e32 v4, v4, v7
	ds_swizzle_b32 v7, v4 offset:swizzle(SWAP,4)
	s_waitcnt lgkmcnt(0)
	v_add_f32_e32 v4, v4, v7
	ds_swizzle_b32 v7, v4 offset:swizzle(SWAP,8)
	s_waitcnt lgkmcnt(0)
	v_add_f32_e32 v4, v4, v7
	ds_swizzle_b32 v7, v4 offset:swizzle(SWAP,16)
	s_waitcnt lgkmcnt(0)
	v_add_f32_e32 v4, v4, v7
	v_mov_b32_e32 v7, v4
	s_nop 1
	v_permlane32_swap_b32_e32 v4, v7
	v_add_f32_e32 v4, v4, v7
	v_fmamk_f32 v4, v4, 0x3a000000, v129
	v_mul_f32_e32 v7, 0x4f800000, v4
	v_cmp_gt_f32_e32 vcc, s28, v4
	s_nop 1
	v_cndmask_b32_e32 v4, v4, v7, vcc
	v_sqrt_f32_e32 v7, v4
	s_nop 0
	v_add_u32_e32 v9, -1, v7
	v_add_u32_e32 v11, 1, v7
	v_fma_f32 v13, -v9, v7, v4
	v_fma_f32 v15, -v11, v7, v4
	v_cmp_ge_f32_e64 s[0:1], 0, v13
	s_nop 1
	v_cndmask_b32_e64 v7, v7, v9, s[0:1]
	v_cmp_lt_f32_e64 s[0:1], 0, v15
	s_nop 1
	v_cndmask_b32_e64 v7, v7, v11, s[0:1]
	v_mul_f32_e32 v9, 0x37800000, v7
	v_cndmask_b32_e32 v7, v7, v9, vcc
	v_cmp_class_f32_e32 vcc, v4, v130
	s_nop 1
	v_cndmask_b32_e32 v4, v7, v4, vcc
	v_div_scale_f32 v7, s[0:1], v4, v4, 1.0
	v_rcp_f32_e32 v11, v7
	v_div_scale_f32 v9, vcc, 1.0, v4, 1.0
	v_fma_f32 v13, -v7, v11, 1.0
	v_fmac_f32_e32 v11, v13, v11
	v_mul_f32_e32 v13, v9, v11
	v_fma_f32 v15, -v7, v13, v9
	v_fmac_f32_e32 v13, v15, v11
	v_fma_f32 v7, -v7, v13, v9
	v_div_fmas_f32 v7, v7, v11, v13
	v_div_fixup_f32 v4, v7, v4, 1.0
	v_pk_mul_f32 v[0:1], v[4:5], v[0:1] op_sel_hi:[0,1]
	v_pk_mul_f32 v[2:3], v[4:5], v[2:3] op_sel_hi:[0,1]
	s_waitcnt vmcnt(0)
	v_pk_mul_f32 v[2:3], v[2:3], v[92:93]
	v_pk_mul_f32 v[0:1], v[0:1], v[90:91]
	global_store_dwordx4 v[122:123], v[0:3], off
	global_load_dwordx4 v[0:3], v6, s[4:5]
	v_pk_mul_f32 v[6:7], v[4:5], v[26:27] op_sel_hi:[0,1]
	v_pk_mul_f32 v[26:27], v[4:5], v[28:29] op_sel_hi:[0,1]
	s_waitcnt vmcnt(0)
	v_pk_mul_f32 v[0:1], v[26:27], v[0:1]
	v_pk_mul_f32 v[2:3], v[6:7], v[2:3]
	global_store_dwordx4 v[124:125], v[0:3], off
	global_load_dwordx4 v[0:3], v8, s[4:5]
	v_pk_mul_f32 v[6:7], v[4:5], v[30:31] op_sel_hi:[0,1]
	v_pk_mul_f32 v[8:9], v[4:5], v[32:33] op_sel_hi:[0,1]
	s_waitcnt vmcnt(0)
	v_pk_mul_f32 v[0:1], v[8:9], v[0:1]
	v_pk_mul_f32 v[2:3], v[6:7], v[2:3]
	global_store_dwordx4 v[132:133], v[0:3], off
	global_load_dwordx4 v[0:3], v10, s[4:5]
	v_pk_mul_f32 v[6:7], v[4:5], v[34:35] op_sel_hi:[0,1]
	v_pk_mul_f32 v[8:9], v[4:5], v[36:37] op_sel_hi:[0,1]
	s_waitcnt vmcnt(0)
	v_pk_mul_f32 v[0:1], v[8:9], v[0:1]
	v_pk_mul_f32 v[2:3], v[6:7], v[2:3]
	global_store_dwordx4 v[134:135], v[0:3], off
	global_load_dwordx4 v[0:3], v12, s[4:5]
	v_pk_mul_f32 v[6:7], v[4:5], v[38:39] op_sel_hi:[0,1]
	v_pk_mul_f32 v[8:9], v[4:5], v[40:41] op_sel_hi:[0,1]
	s_waitcnt vmcnt(0)
	v_pk_mul_f32 v[0:1], v[8:9], v[0:1]
	v_pk_mul_f32 v[2:3], v[6:7], v[2:3]
	global_store_dwordx4 v[136:137], v[0:3], off
	global_load_dwordx4 v[0:3], v14, s[4:5]
	v_pk_mul_f32 v[6:7], v[4:5], v[42:43] op_sel_hi:[0,1]
	v_pk_mul_f32 v[8:9], v[4:5], v[44:45] op_sel_hi:[0,1]
	s_waitcnt vmcnt(0)
	v_pk_mul_f32 v[0:1], v[8:9], v[0:1]
	v_pk_mul_f32 v[2:3], v[6:7], v[2:3]
	global_store_dwordx4 v[24:25], v[0:3], off
	global_load_dwordx4 v[0:3], v16, s[4:5]
	v_pk_mul_f32 v[6:7], v[4:5], v[46:47] op_sel_hi:[0,1]
	v_pk_mul_f32 v[8:9], v[4:5], v[48:49] op_sel_hi:[0,1]
	s_waitcnt vmcnt(0)
	v_pk_mul_f32 v[0:1], v[8:9], v[0:1]
	v_pk_mul_f32 v[2:3], v[6:7], v[2:3]
	global_store_dwordx4 v[22:23], v[0:3], off
	global_load_dwordx4 v[0:3], v18, s[4:5]
	v_pk_mul_f32 v[6:7], v[4:5], v[50:51] op_sel_hi:[0,1]
	v_pk_mul_f32 v[8:9], v[4:5], v[52:53] op_sel_hi:[0,1]
	s_waitcnt vmcnt(0)
	v_pk_mul_f32 v[0:1], v[8:9], v[0:1]
	v_pk_mul_f32 v[2:3], v[6:7], v[2:3]
	global_store_dwordx4 v[20:21], v[0:3], off
	s_cbranch_scc1 .LBB0_1206
